# gate/up LIVE1 K-loop head: last-iteration flag (s_cmp_eq + s_cselect_b64) moved behind the first eight fragment reads; only the branch test stays at the loop head
# speedup vs baseline: 1.0031x; 1.0031x over previous
.LBB0_1244:
	s_cmp_lg_u32 s44, 28
	s_cbranch_scc1 .LBB0_1246
	ds_read_u16 v137, v135
	ds_read_u16 v139, v135 offset:256
	ds_read_u16 v141, v136
	ds_read_u16 v142, v136 offset:256
	s_waitcnt lgkmcnt(3)
	v_lshl_or_b32 v138, v137, 12, v147
	s_waitcnt lgkmcnt(2)
	v_lshl_or_b32 v140, v139, 12, v147
	s_waitcnt lgkmcnt(1)
	v_lshl_or_b32 v137, v141, 12, v147
	s_waitcnt lgkmcnt(0)
	v_lshl_or_b32 v139, v142, 12, v147
.LBB0_1246:
	ds_read_b128 v[142:145], v247
	ds_read_b128 v[172:175], v247 offset:1024
	ds_read_b128 v[176:179], v247 offset:2048
	ds_read_b128 v[180:183], v247 offset:3072
	ds_read_b128 v[184:187], v248
	ds_read_b128 v[188:191], v248 offset:1024
	ds_read_b128 v[196:199], v248 offset:2048
	ds_read_b128 v[200:203], v248 offset:3072
	s_cmp_eq_u32 s44, 28
	s_cselect_b64 s[42:43], -1, 0
	s_add_u32 s38, s18, 0x100
	s_addc_u32 s39, s19, 0
	s_add_i32 s85, s29, s18
	s_and_b64 s[14:15], s[42:43], exec
	s_cselect_b32 s45, 0, s38
	s_add_i32 s14, s18, 0x80
	s_mov_b32 m0, s79
	ds_read_b128 v[204:207], v156
	ds_read_b128 v[208:211], v156 offset:1024
	ds_read_b128 v[212:215], v156 offset:2048
	ds_read_b128 v[216:219], v156 offset:3072
	ds_read_b128 v[220:223], v156 offset:4096
	ds_read_b128 v[224:227], v156 offset:5120
	ds_read_b128 v[228:231], v156 offset:6144
	ds_read_b128 v[232:235], v156 offset:7168
	buffer_load_dwordx4 v132, s[8:11], s14 offen lds
	s_mov_b32 m0, s80
	s_nop 0
	buffer_load_dwordx4 v134, s[8:11], s14 offen lds
	s_waitcnt vmcnt(8)
	s_waitcnt lgkmcnt(0)
	s_barrier
	v_mfma_f32_16x16x32_bf16 v[126:129], v[142:145], v[204:207], v[126:129]
	v_mfma_f32_16x16x32_bf16 v[122:125], v[176:179], v[204:207], v[122:125]
	v_mfma_f32_16x16x32_bf16 v[102:105], v[142:145], v[212:215], v[102:105]
	v_mfma_f32_16x16x32_bf16 v[90:93], v[176:179], v[212:215], v[90:93]
	v_mfma_f32_16x16x32_bf16 v[70:73], v[142:145], v[220:223], v[70:73]
	v_mfma_f32_16x16x32_bf16 v[58:61], v[176:179], v[220:223], v[58:61]
	v_mfma_f32_16x16x32_bf16 v[38:41], v[142:145], v[228:231], v[38:41]
	v_mfma_f32_16x16x32_bf16 v[26:29], v[176:179], v[228:231], v[26:29]
	v_mfma_f32_16x16x32_bf16 v[118:121], v[184:187], v[204:207], v[118:121]
	v_mfma_f32_16x16x32_bf16 v[110:113], v[196:199], v[204:207], v[110:113]
	v_mfma_f32_16x16x32_bf16 v[86:89], v[184:187], v[212:215], v[86:89]
	v_mfma_f32_16x16x32_bf16 v[74:77], v[196:199], v[212:215], v[74:77]
	v_mfma_f32_16x16x32_bf16 v[54:57], v[184:187], v[220:223], v[54:57]
	v_mfma_f32_16x16x32_bf16 v[42:45], v[196:199], v[220:223], v[42:45]
	v_mfma_f32_16x16x32_bf16 v[22:25], v[184:187], v[228:231], v[22:25]
	v_mfma_f32_16x16x32_bf16 v[10:13], v[196:199], v[228:231], v[10:13]
	v_mfma_f32_16x16x32_bf16 v[126:129], v[172:175], v[208:211], v[126:129]
	v_mfma_f32_16x16x32_bf16 v[122:125], v[180:183], v[208:211], v[122:125]
	v_mfma_f32_16x16x32_bf16 v[102:105], v[172:175], v[216:219], v[102:105]
	v_mfma_f32_16x16x32_bf16 v[90:93], v[180:183], v[216:219], v[90:93]
	v_mfma_f32_16x16x32_bf16 v[70:73], v[172:175], v[224:227], v[70:73]
	v_mfma_f32_16x16x32_bf16 v[58:61], v[180:183], v[224:227], v[58:61]
	v_mfma_f32_16x16x32_bf16 v[38:41], v[172:175], v[232:235], v[38:41]
	v_mfma_f32_16x16x32_bf16 v[26:29], v[180:183], v[232:235], v[26:29]
	v_mfma_f32_16x16x32_bf16 v[118:121], v[188:191], v[208:211], v[118:121]
	v_mfma_f32_16x16x32_bf16 v[110:113], v[200:203], v[208:211], v[110:113]
	v_mfma_f32_16x16x32_bf16 v[86:89], v[188:191], v[216:219], v[86:89]
	v_mfma_f32_16x16x32_bf16 v[74:77], v[200:203], v[216:219], v[74:77]
	v_mfma_f32_16x16x32_bf16 v[54:57], v[188:191], v[224:227], v[54:57]
	v_mfma_f32_16x16x32_bf16 v[42:45], v[200:203], v[224:227], v[42:45]
	v_mfma_f32_16x16x32_bf16 v[22:25], v[188:191], v[232:235], v[22:25]
	v_mfma_f32_16x16x32_bf16 v[10:13], v[200:203], v[232:235], v[10:13]
	s_barrier
	s_and_b64 s[14:15], s[42:43], exec
	s_cselect_b32 s14, s5, s85
	s_mov_b32 m0, s66
	s_mov_b32 s18, s10
	s_mov_b32 s19, s11
	s_sub_i32 s14, s14, s16
	ds_read_b128 v[204:207], v156 offset:16384
	ds_read_b128 v[208:211], v156 offset:17408
	ds_read_b128 v[212:215], v156 offset:18432
	ds_read_b128 v[216:219], v156 offset:19456
	ds_read_b128 v[220:223], v156 offset:20480
	ds_read_b128 v[224:227], v156 offset:21504
	ds_read_b128 v[228:231], v156 offset:22528
	ds_read_b128 v[232:235], v156 offset:23552
	buffer_load_dwordx4 v151, s[16:19], s14 offen lds
	s_mov_b32 m0, s67
	s_add_i32 s15, s14, 0x80000
	buffer_load_dwordx4 v158, s[16:19], s14 offen lds
	s_mov_b32 m0, s68
	s_nop 0
	buffer_load_dwordx4 v151, s[16:19], s15 offen lds
	s_mov_b32 m0, s69
	s_nop 0
	buffer_load_dwordx4 v158, s[16:19], s15 offen lds
	s_mov_b32 m0, s65
	s_nop 0
	buffer_load_dwordx4 v138, s[8:11], s45 offen lds
	s_mov_b32 m0, s70
	s_nop 0
	buffer_load_dwordx4 v137, s[8:11], s45 offen lds
	s_waitcnt vmcnt(8)
	s_waitcnt lgkmcnt(0)
	s_barrier
	v_mfma_f32_16x16x32_bf16 v[114:117], v[142:145], v[204:207], v[114:117]
	v_mfma_f32_16x16x32_bf16 v[98:101], v[176:179], v[204:207], v[98:101]
	v_mfma_f32_16x16x32_bf16 v[82:85], v[142:145], v[212:215], v[82:85]
	v_mfma_f32_16x16x32_bf16 v[66:69], v[176:179], v[212:215], v[66:69]
	v_mfma_f32_16x16x32_bf16 v[50:53], v[142:145], v[220:223], v[50:53]
	v_mfma_f32_16x16x32_bf16 v[34:37], v[176:179], v[220:223], v[34:37]
	v_mfma_f32_16x16x32_bf16 v[18:21], v[142:145], v[228:231], v[18:21]
	v_mfma_f32_16x16x32_bf16 v[6:9], v[176:179], v[228:231], v[6:9]
	v_mfma_f32_16x16x32_bf16 v[106:109], v[184:187], v[204:207], v[106:109]
	v_mfma_f32_16x16x32_bf16 v[94:97], v[196:199], v[204:207], v[94:97]
	v_mfma_f32_16x16x32_bf16 v[78:81], v[184:187], v[212:215], v[78:81]
	v_mfma_f32_16x16x32_bf16 v[62:65], v[196:199], v[212:215], v[62:65]
	v_mfma_f32_16x16x32_bf16 v[46:49], v[184:187], v[220:223], v[46:49]
	v_mfma_f32_16x16x32_bf16 v[30:33], v[196:199], v[220:223], v[30:33]
	v_mfma_f32_16x16x32_bf16 v[14:17], v[184:187], v[228:231], v[14:17]
	v_mfma_f32_16x16x32_bf16 v[2:5], v[196:199], v[228:231], v[2:5]
	v_mfma_f32_16x16x32_bf16 v[114:117], v[172:175], v[208:211], v[114:117]
	v_mfma_f32_16x16x32_bf16 v[98:101], v[180:183], v[208:211], v[98:101]
	v_mfma_f32_16x16x32_bf16 v[82:85], v[172:175], v[216:219], v[82:85]
	v_mfma_f32_16x16x32_bf16 v[66:69], v[180:183], v[216:219], v[66:69]
	v_mfma_f32_16x16x32_bf16 v[50:53], v[172:175], v[224:227], v[50:53]
	v_mfma_f32_16x16x32_bf16 v[34:37], v[180:183], v[224:227], v[34:37]
	v_mfma_f32_16x16x32_bf16 v[18:21], v[172:175], v[232:235], v[18:21]
	v_mfma_f32_16x16x32_bf16 v[6:9], v[180:183], v[232:235], v[6:9]
	v_mfma_f32_16x16x32_bf16 v[106:109], v[188:191], v[208:211], v[106:109]
	v_mfma_f32_16x16x32_bf16 v[94:97], v[200:203], v[208:211], v[94:97]
	v_mfma_f32_16x16x32_bf16 v[78:81], v[188:191], v[216:219], v[78:81]
	v_mfma_f32_16x16x32_bf16 v[62:65], v[200:203], v[216:219], v[62:65]
	v_mfma_f32_16x16x32_bf16 v[46:49], v[188:191], v[224:227], v[46:49]
	v_mfma_f32_16x16x32_bf16 v[30:33], v[200:203], v[224:227], v[30:33]
	v_mfma_f32_16x16x32_bf16 v[14:17], v[188:191], v[232:235], v[14:17]
	v_mfma_f32_16x16x32_bf16 v[2:5], v[200:203], v[232:235], v[2:5]
	s_barrier
	ds_read_b128 v[142:145], v249
	ds_read_b128 v[172:175], v249 offset:1024
	ds_read_b128 v[176:179], v249 offset:2048
	ds_read_b128 v[180:183], v249 offset:3072
	ds_read_b128 v[184:187], v250
	ds_read_b128 v[188:191], v250 offset:1024
	ds_read_b128 v[196:199], v250 offset:2048
	ds_read_b128 v[200:203], v250 offset:3072
	s_mov_b32 m0, s71
	ds_read_b128 v[204:207], v156 offset:32768
	ds_read_b128 v[208:211], v156 offset:33792
	ds_read_b128 v[212:215], v156 offset:34816
	ds_read_b128 v[216:219], v156 offset:35840
	ds_read_b128 v[220:223], v156 offset:36864
	ds_read_b128 v[224:227], v156 offset:37888
	ds_read_b128 v[228:231], v156 offset:38912
	ds_read_b128 v[232:235], v156 offset:39936
	buffer_load_dwordx4 v140, s[8:11], s45 offen lds
	s_mov_b32 m0, s72
	s_nop 0
	buffer_load_dwordx4 v139, s[8:11], s45 offen lds
	s_waitcnt vmcnt(8)
	s_waitcnt lgkmcnt(0)
	s_barrier
	v_mfma_f32_16x16x32_bf16 v[126:129], v[142:145], v[204:207], v[126:129]
	v_mfma_f32_16x16x32_bf16 v[122:125], v[176:179], v[204:207], v[122:125]
	v_mfma_f32_16x16x32_bf16 v[102:105], v[142:145], v[212:215], v[102:105]
	v_mfma_f32_16x16x32_bf16 v[90:93], v[176:179], v[212:215], v[90:93]
	v_mfma_f32_16x16x32_bf16 v[70:73], v[142:145], v[220:223], v[70:73]
	v_mfma_f32_16x16x32_bf16 v[58:61], v[176:179], v[220:223], v[58:61]
	v_mfma_f32_16x16x32_bf16 v[38:41], v[142:145], v[228:231], v[38:41]
	v_mfma_f32_16x16x32_bf16 v[26:29], v[176:179], v[228:231], v[26:29]
	v_mfma_f32_16x16x32_bf16 v[118:121], v[184:187], v[204:207], v[118:121]
	v_mfma_f32_16x16x32_bf16 v[110:113], v[196:199], v[204:207], v[110:113]
	v_mfma_f32_16x16x32_bf16 v[86:89], v[184:187], v[212:215], v[86:89]
	v_mfma_f32_16x16x32_bf16 v[74:77], v[196:199], v[212:215], v[74:77]
	v_mfma_f32_16x16x32_bf16 v[54:57], v[184:187], v[220:223], v[54:57]
	v_mfma_f32_16x16x32_bf16 v[42:45], v[196:199], v[220:223], v[42:45]
	v_mfma_f32_16x16x32_bf16 v[22:25], v[184:187], v[228:231], v[22:25]
	v_mfma_f32_16x16x32_bf16 v[10:13], v[196:199], v[228:231], v[10:13]
	v_mfma_f32_16x16x32_bf16 v[126:129], v[172:175], v[208:211], v[126:129]
	v_mfma_f32_16x16x32_bf16 v[122:125], v[180:183], v[208:211], v[122:125]
	v_mfma_f32_16x16x32_bf16 v[102:105], v[172:175], v[216:219], v[102:105]
	v_mfma_f32_16x16x32_bf16 v[90:93], v[180:183], v[216:219], v[90:93]
	v_mfma_f32_16x16x32_bf16 v[70:73], v[172:175], v[224:227], v[70:73]
	v_mfma_f32_16x16x32_bf16 v[58:61], v[180:183], v[224:227], v[58:61]
	v_mfma_f32_16x16x32_bf16 v[38:41], v[172:175], v[232:235], v[38:41]
	v_mfma_f32_16x16x32_bf16 v[26:29], v[180:183], v[232:235], v[26:29]
	v_mfma_f32_16x16x32_bf16 v[118:121], v[188:191], v[208:211], v[118:121]
	v_mfma_f32_16x16x32_bf16 v[110:113], v[200:203], v[208:211], v[110:113]
	v_mfma_f32_16x16x32_bf16 v[86:89], v[188:191], v[216:219], v[86:89]
	v_mfma_f32_16x16x32_bf16 v[74:77], v[200:203], v[216:219], v[74:77]
	v_mfma_f32_16x16x32_bf16 v[54:57], v[188:191], v[224:227], v[54:57]
	v_mfma_f32_16x16x32_bf16 v[42:45], v[200:203], v[224:227], v[42:45]
	v_mfma_f32_16x16x32_bf16 v[22:25], v[188:191], v[232:235], v[22:25]
	v_mfma_f32_16x16x32_bf16 v[10:13], v[200:203], v[232:235], v[10:13]
	s_barrier
	s_mov_b32 m0, s73
	s_add_i32 s15, s14, 0x80
	ds_read_b128 v[204:207], v156 offset:49152
	ds_read_b128 v[208:211], v156 offset:50176
	ds_read_b128 v[212:215], v156 offset:51200
	ds_read_b128 v[216:219], v156 offset:52224
	ds_read_b128 v[220:223], v156 offset:53248
	ds_read_b128 v[224:227], v156 offset:54272
	ds_read_b128 v[228:231], v156 offset:55296
	ds_read_b128 v[232:235], v156 offset:56320
	buffer_load_dwordx4 v151, s[16:19], s15 offen lds
	s_mov_b32 m0, s74
	s_add_i32 s14, s14, 0x80080
	buffer_load_dwordx4 v158, s[16:19], s15 offen lds
	s_mov_b32 m0, s77
	s_bitset1_b32 s45, 7
	buffer_load_dwordx4 v151, s[16:19], s14 offen lds
	s_mov_b32 m0, s78
	s_nop 0
	buffer_load_dwordx4 v158, s[16:19], s14 offen lds
	s_mov_b32 m0, s75
	s_nop 0
	buffer_load_dwordx4 v138, s[8:11], s45 offen lds
	s_mov_b32 m0, s76
	s_nop 0
	buffer_load_dwordx4 v137, s[8:11], s45 offen lds
	s_waitcnt vmcnt(8)
	s_waitcnt lgkmcnt(0)
	s_barrier
	v_mfma_f32_16x16x32_bf16 v[114:117], v[142:145], v[204:207], v[114:117]
	v_mfma_f32_16x16x32_bf16 v[98:101], v[176:179], v[204:207], v[98:101]
	v_mfma_f32_16x16x32_bf16 v[82:85], v[142:145], v[212:215], v[82:85]
	v_mfma_f32_16x16x32_bf16 v[66:69], v[176:179], v[212:215], v[66:69]
	v_mfma_f32_16x16x32_bf16 v[50:53], v[142:145], v[220:223], v[50:53]
	v_mfma_f32_16x16x32_bf16 v[34:37], v[176:179], v[220:223], v[34:37]
	v_mfma_f32_16x16x32_bf16 v[18:21], v[142:145], v[228:231], v[18:21]
	v_mfma_f32_16x16x32_bf16 v[6:9], v[176:179], v[228:231], v[6:9]
	v_mfma_f32_16x16x32_bf16 v[106:109], v[184:187], v[204:207], v[106:109]
	v_mfma_f32_16x16x32_bf16 v[94:97], v[196:199], v[204:207], v[94:97]
	v_mfma_f32_16x16x32_bf16 v[78:81], v[184:187], v[212:215], v[78:81]
	v_mfma_f32_16x16x32_bf16 v[62:65], v[196:199], v[212:215], v[62:65]
	v_mfma_f32_16x16x32_bf16 v[46:49], v[184:187], v[220:223], v[46:49]
	v_mfma_f32_16x16x32_bf16 v[30:33], v[196:199], v[220:223], v[30:33]
	v_mfma_f32_16x16x32_bf16 v[14:17], v[184:187], v[228:231], v[14:17]
	v_mfma_f32_16x16x32_bf16 v[2:5], v[196:199], v[228:231], v[2:5]
	v_mfma_f32_16x16x32_bf16 v[114:117], v[172:175], v[208:211], v[114:117]
	v_mfma_f32_16x16x32_bf16 v[98:101], v[180:183], v[208:211], v[98:101]
	v_mfma_f32_16x16x32_bf16 v[82:85], v[172:175], v[216:219], v[82:85]
	v_mfma_f32_16x16x32_bf16 v[66:69], v[180:183], v[216:219], v[66:69]
	v_mfma_f32_16x16x32_bf16 v[50:53], v[172:175], v[224:227], v[50:53]
	v_mfma_f32_16x16x32_bf16 v[34:37], v[180:183], v[224:227], v[34:37]
	v_mfma_f32_16x16x32_bf16 v[18:21], v[172:175], v[232:235], v[18:21]
	v_mfma_f32_16x16x32_bf16 v[6:9], v[180:183], v[232:235], v[6:9]
	v_mfma_f32_16x16x32_bf16 v[106:109], v[188:191], v[208:211], v[106:109]
	v_mfma_f32_16x16x32_bf16 v[94:97], v[200:203], v[208:211], v[94:97]
	v_mfma_f32_16x16x32_bf16 v[78:81], v[188:191], v[216:219], v[78:81]
	v_mfma_f32_16x16x32_bf16 v[62:65], v[200:203], v[216:219], v[62:65]
	v_mfma_f32_16x16x32_bf16 v[46:49], v[188:191], v[224:227], v[46:49]
	v_mfma_f32_16x16x32_bf16 v[30:33], v[200:203], v[224:227], v[30:33]
	v_mfma_f32_16x16x32_bf16 v[14:17], v[188:191], v[232:235], v[14:17]
	v_mfma_f32_16x16x32_bf16 v[2:5], v[200:203], v[232:235], v[2:5]
	s_barrier
	s_add_i32 s44, s44, 2
	s_cmp_gt_u32 s44, 29
	s_cbranch_scc1 .LBB0_1248
	s_mov_b64 s[18:19], s[38:39]
	s_branch .LBB0_1244
